# stack10 + attention tile loop: waves 4-7 take the per-tile barrier before the VALU tail (half-tile stagger of SIMD partners), one barrier per wave per tile kept
# baseline (speedup 1.0000x reference)
; #define LAS __attribute__((address_space(3)))
; __device__ __forceinline__ float half_swap_max(float m) { unsigned a = __builtin_bit_cast(unsigned, m), b = a; half_swap(a, b); return __builtin_fmaxf(__builtin_bit_cast(float, a), __builtin_bit_cast(float, b)); }
; #define EX2(P, i) do { P[i] = __builtin_amdgcn_exp2f(P[i]); P[(i) + 1] = __builtin_amdgcn_exp2f(P[(i) + 1]); } while (0)
; #define PK8(P, i) ({ v4u w_; w_.x = pk2(P[i], P[(i) + 1]); w_.y = pk2(P[(i) + 2], P[(i) + 3]); w_.z = pk2(P[(i) + 4], P[(i) + 5]); w_.w = pk2(P[(i) + 6], P[(i) + 7]); __builtin_bit_cast(bf16x8, w_); })
; __device__ __forceinline__ void attn_unit(LAS unsigned char* lds, const bf16* proj, bf16* Y, const float* relb, const float* hgain, float lam, float oscale, int b, int h, int qb, int tid, int lane, int wid, Stopwatch& sw) {
;     ...
;       float mt = __builtin_fmaxf(sA0[0], sA1[0]);
; #pragma unroll
;       for (int r = 1; r < 16; ++r) mt = __builtin_fmaxf(mt, __builtin_fmaxf(sA0[r], sA1[r]));
;       mt = half_swap_max(mt); m_run = mt;
; #pragma unroll
;       for (int r = 0; r < 16; ++r) { sA0[r] -= mt; sA1[r] -= mt; } }
;     int sc = 0, sn = 32768, sn2 = 65536;
;     ...
;     bf16x8 qreg[4];
; #pragma unroll
;     for (int d0 = 0; d0 < 4; ++d0) qreg[d0] = *(const LAS bf16x8*)(qlds + d0 * 1024);
;     bf16x8 pw0, pw1, pw2, pw3;
;     {
; #pragma unroll
;       for (int r = 0; r < 16; r += 2) { EX2(sA0, r); EX2(sA1, r); }
;       float sm_ = 0.f;
; #pragma unroll
;       for (int r = 0; r < 16; ++r) sm_ += sA0[r] + sA1[r];
;       l_run += sm_; pw0 = PK8(sA0, 0); pw1 = PK8(sA0, 8); pw2 = PK8(sA1, 0); pw3 = PK8(sA1, 8); }
.LBB0_394:
	v_and_b32_e32 v166, 63, v61
	v_lshrrev_b32_e32 v36, 2, v61
	v_lshlrev_b32_e32 v41, 3, v166
	v_and_b32_e32 v36, 11, v36
	v_lshrrev_b32_e32 v37, 3, v61
	v_and_b32_e32 v38, 1, v63
	v_and_b32_e32 v41, 8, v41
	v_and_or_b32 v37, v37, 2, v38
	v_lshrrev_b32_e32 v39, 2, v36
	v_lshl_or_b32 v42, v36, 8, v41
	v_or_b32_e32 v36, 4, v36
	v_and_b32_e32 v38, 12, v61
	v_lshrrev_b32_e32 v43, 2, v36
	v_lshl_or_b32 v41, v36, 8, v41
	v_or_b32_e32 v36, 4, v37
	v_bitop3_b32 v46, v43, v36, v38 bitop3:0x36
	v_or_b32_e32 v36, 8, v37
	v_or_b32_e32 v40, v39, v38
	v_bitop3_b32 v48, v43, v36, v38 bitop3:0x36
	v_or_b32_e32 v36, 12, v37
	v_bitop3_b32 v39, v39, v37, v38 bitop3:0x36
	v_bitop3_b32 v44, v43, v37, v38 bitop3:0x36
	v_bitop3_b32 v45, v37, v40, 4 bitop3:0x36
	v_bitop3_b32 v47, v37, v40, 8 bitop3:0x36
	v_bitop3_b32 v40, v37, v40, 12 bitop3:0x36
	v_bitop3_b32 v38, v43, v36, v38 bitop3:0x36
	v_max_f32_e32 v36, v5, v5
	v_max_f32_e32 v37, v21, v21
	v_max_f32_e32 v36, v37, v36
	v_max_f32_e32 v37, v6, v6
	v_max_f32_e32 v43, v22, v22
	v_max_f32_e32 v37, v43, v37
	v_max_f32_e32 v43, v7, v7
	v_max_f32_e32 v49, v23, v23
	v_max3_f32 v36, v20, v4, v36
	v_max_f32_e32 v43, v49, v43
	v_max3_f32 v36, v36, v37, v43
	v_max_f32_e32 v37, v8, v8
	v_max_f32_e32 v43, v24, v24
	v_max_f32_e32 v37, v43, v37
	v_max_f32_e32 v43, v9, v9
	v_max_f32_e32 v49, v25, v25
	v_max_f32_e32 v43, v49, v43
	v_max3_f32 v36, v36, v37, v43
	v_max_f32_e32 v37, v10, v10
	v_max_f32_e32 v43, v26, v26
	v_max_f32_e32 v37, v43, v37
	v_max_f32_e32 v43, v11, v11
	v_max_f32_e32 v49, v27, v27
	v_max_f32_e32 v43, v49, v43
	v_max3_f32 v36, v36, v37, v43
	v_max_f32_e32 v37, v12, v12
	v_max_f32_e32 v43, v28, v28
	v_max_f32_e32 v37, v43, v37
	v_max_f32_e32 v43, v13, v13
	v_max_f32_e32 v49, v29, v29
	v_max_f32_e32 v43, v49, v43
	v_max3_f32 v36, v36, v37, v43
	v_max_f32_e32 v37, v14, v14
	v_max_f32_e32 v43, v30, v30
	v_max_f32_e32 v37, v43, v37
	v_max_f32_e32 v43, v15, v15
	v_max_f32_e32 v49, v31, v31
	v_max_f32_e32 v43, v49, v43
	v_max3_f32 v36, v36, v37, v43
	v_max_f32_e32 v37, v16, v16
	v_max_f32_e32 v43, v32, v32
	v_max_f32_e32 v37, v43, v37
	v_max_f32_e32 v43, v17, v17
	v_max_f32_e32 v49, v33, v33
	v_max_f32_e32 v43, v49, v43
	v_max3_f32 v36, v36, v37, v43
	v_max_f32_e32 v37, v18, v18
	v_max_f32_e32 v43, v34, v34
	v_max_f32_e32 v37, v43, v37
	v_max_f32_e32 v43, v19, v19
	v_max_f32_e32 v49, v35, v35
	v_max_f32_e32 v43, v49, v43
	v_max3_f32 v36, v36, v37, v43
	v_mov_b32_e32 v37, v36
	s_nop 1
	v_permlane32_swap_b32 v36, v37
	s_nop 1
	ds_read_b128 v[116:119], v62
	ds_read_b128 v[120:123], v62 offset:1024
	ds_read_b128 v[124:127], v62 offset:2048
	ds_read_b128 v[128:131], v62 offset:3072
	v_max_f32_e32 v37, v37, v37
	v_max_f32_e32 v36, v36, v36
	v_max_f32_e32 v167, v36, v37
	v_sub_f32_e32 v20, v20, v167
	v_sub_f32_e32 v36, v4, v167
	v_sub_f32_e32 v4, v21, v167
	v_sub_f32_e32 v5, v5, v167
	v_exp_f32_e32 v62, v20
	v_exp_f32_e32 v63, v36
	v_sub_f32_e32 v21, v22, v167
	v_sub_f32_e32 v22, v6, v167
	v_exp_f32_e32 v4, v4
	v_exp_f32_e32 v6, v5
	v_sub_f32_e32 v23, v23, v167
	v_sub_f32_e32 v7, v7, v167
	v_exp_f32_e32 v64, v21
	v_exp_f32_e32 v65, v22
	v_sub_f32_e32 v37, v8, v167
	v_sub_f32_e32 v43, v10, v167
	v_exp_f32_e32 v8, v23
	v_exp_f32_e32 v10, v7
	v_add_f32_e32 v5, v62, v63
	v_mov_b32_e32 v7, v3
	v_sub_f32_e32 v24, v24, v167
	v_exp_f32_e32 v67, v37
	v_pk_add_f32 v[36:37], v[4:5], v[6:7]
	v_sub_f32_e32 v25, v25, v167
	v_sub_f32_e32 v9, v9, v167
	v_sub_f32_e32 v11, v11, v167
	v_exp_f32_e32 v66, v24
	v_pk_add_f32 v[36:37], v[36:37], v[36:37] op_sel_hi:[0,1]
	v_sub_f32_e32 v49, v12, v167
	v_sub_f32_e32 v50, v14, v167
	v_sub_f32_e32 v61, v18, v167
	v_exp_f32_e32 v12, v25
	v_exp_f32_e32 v14, v9
	v_exp_f32_e32 v18, v11
	v_add_f32_e32 v9, v64, v65
	v_mov_b32_e32 v11, v37
	v_sub_f32_e32 v26, v26, v167
	v_pk_add_f32 v[36:37], v[8:9], v[10:11]
	v_sub_f32_e32 v27, v27, v167
	v_sub_f32_e32 v13, v13, v167
	v_sub_f32_e32 v15, v15, v167
	v_exp_f32_e32 v68, v26
	v_exp_f32_e32 v43, v43
	v_pk_add_f32 v[36:37], v[36:37], v[36:37] op_sel_hi:[0,1]
	v_sub_f32_e32 v51, v16, v167
	v_exp_f32_e32 v16, v27
	v_exp_f32_e32 v22, v13
	v_exp_f32_e32 v26, v15
	v_add_f32_e32 v13, v66, v67
; #define LAS __attribute__((address_space(3)))
; #define EX2(P, i) do { P[i] = __builtin_amdgcn_exp2f(P[i]); P[(i) + 1] = __builtin_amdgcn_exp2f(P[(i) + 1]); } while (0)
; #define PK8(P, i) ({ v4u w_; w_.x = pk2(P[i], P[(i) + 1]); w_.y = pk2(P[(i) + 2], P[(i) + 3]); w_.z = pk2(P[(i) + 4], P[(i) + 5]); w_.w = pk2(P[(i) + 6], P[(i) + 7]); __builtin_bit_cast(bf16x8, w_); })
; __device__ __forceinline__ void attn_unit(LAS unsigned char* lds, const bf16* proj, bf16* Y, const float* relb, const float* hgain, float lam, float oscale, int b, int h, int qb, int tid, int lane, int wid, Stopwatch& sw) {
;     ...
;     float m_run = -1e30f, l_run = 0.f;
;     f32x16 o[4];
; #pragma unroll
;     for (int c = 0; c < 4; ++c) o[c] = splat16(0.f);
;     const int qi = qw + r32;
;     ...
;     bf16x8 qreg[4];
; #pragma unroll
;     for (int d0 = 0; d0 < 4; ++d0) qreg[d0] = *(const LAS bf16x8*)(qlds + d0 * 1024);
;     bf16x8 pw0, pw1, pw2, pw3;
;     {
; #pragma unroll
;       for (int r = 0; r < 16; r += 2) { EX2(sA0, r); EX2(sA1, r); }
;       float sm_ = 0.f;
; #pragma unroll
;       for (int r = 0; r < 16; ++r) sm_ += sA0[r] + sA1[r];
;       l_run += sm_; pw0 = PK8(sA0, 0); pw1 = PK8(sA0, 8); pw2 = PK8(sA1, 0); pw3 = PK8(sA1, 8); }
	v_mov_b32_e32 v15, v37
	v_sub_f32_e32 v28, v28, v167
	v_pk_add_f32 v[36:37], v[12:13], v[14:15]
	v_sub_f32_e32 v29, v29, v167
	v_sub_f32_e32 v30, v30, v167
	v_sub_f32_e32 v17, v17, v167
	v_sub_f32_e32 v34, v34, v167
	v_sub_f32_e32 v19, v19, v167
	v_exp_f32_e32 v69, v28
	v_exp_f32_e32 v49, v49
	v_pk_add_f32 v[36:37], v[36:37], v[36:37] op_sel_hi:[0,1]
	v_exp_f32_e32 v20, v29
	v_exp_f32_e32 v70, v30
	v_exp_f32_e32 v30, v17
	v_exp_f32_e32 v72, v34
	v_exp_f32_e32 v34, v19
	v_add_f32_e32 v17, v68, v43
	v_mov_b32_e32 v19, v37
	v_pk_add_f32 v[36:37], v[16:17], v[18:19]
	v_sub_f32_e32 v31, v31, v167
	v_exp_f32_e32 v50, v50
	v_pk_add_f32 v[36:37], v[36:37], v[36:37] op_sel_hi:[0,1]
	v_exp_f32_e32 v24, v31
	v_add_f32_e32 v21, v69, v49
	v_mov_b32_e32 v23, v37
	v_sub_f32_e32 v32, v32, v167
	v_pk_add_f32 v[36:37], v[20:21], v[22:23]
	v_sub_f32_e32 v33, v33, v167
	v_exp_f32_e32 v71, v32
	v_exp_f32_e32 v51, v51
	v_pk_add_f32 v[36:37], v[36:37], v[36:37] op_sel_hi:[0,1]
	v_exp_f32_e32 v28, v33
	v_add_f32_e32 v25, v70, v50
	v_mov_b32_e32 v27, v37
	v_pk_add_f32 v[36:37], v[24:25], v[26:27]
	v_sub_f32_e32 v35, v35, v167
	v_exp_f32_e32 v61, v61
	v_pk_add_f32 v[36:37], v[36:37], v[36:37] op_sel_hi:[0,1]
	v_exp_f32_e32 v32, v35
	v_add_f32_e32 v29, v71, v51
	v_mov_b32_e32 v31, v37
	v_pk_add_f32 v[36:37], v[28:29], v[30:31]
	v_add_f32_e32 v33, v72, v61
	v_pk_add_f32 v[36:37], v[36:37], v[36:37] op_sel_hi:[0,1]
	v_mov_b32_e32 v35, v37
	s_lshl_b32 s18, s0, 7
	v_pk_add_f32 v[36:37], v[32:33], v[34:35]
	s_mov_b64 s[36:37], 0x380000
	v_readlane_b32 s0, v252, 60
	v_add_f32_e32 v5, v36, v37
	v_cvt_pk_bf16_f32 v144, v62, v4
	v_lshl_add_u64 v[160:161], v[52:53], 0, s[36:37]
	v_add_u32_e32 v4, s0, v60
	v_mov_b32_e32 v52, v3
	v_mov_b32_e32 v53, v3
	v_add_f32_e32 v153, 0, v5
	v_cvt_pk_bf16_f32 v145, v64, v8
	v_cvt_pk_bf16_f32 v146, v66, v12
	v_cvt_pk_bf16_f32 v147, v68, v16
	v_cvt_pk_bf16_f32 v140, v69, v20
	v_cvt_pk_bf16_f32 v141, v70, v24
	v_cvt_pk_bf16_f32 v142, v71, v28
	v_cvt_pk_bf16_f32 v143, v72, v32
	v_cvt_pk_bf16_f32 v132, v63, v6
	v_cvt_pk_bf16_f32 v133, v65, v10
	v_cvt_pk_bf16_f32 v134, v67, v14
	v_cvt_pk_bf16_f32 v135, v43, v18
	v_cvt_pk_bf16_f32 v136, v49, v22
	v_cvt_pk_bf16_f32 v137, v50, v26
	v_cvt_pk_bf16_f32 v138, v51, v30
	v_cvt_pk_bf16_f32 v139, v61, v34
	v_lshl_or_b32 v175, v39, 4, v42
	v_lshl_or_b32 v174, v44, 4, v41
	v_lshl_or_b32 v173, v45, 4, v42
	v_lshl_or_b32 v172, v46, 4, v41
	v_lshl_or_b32 v171, v47, 4, v42
	v_lshl_or_b32 v170, v48, 4, v41
	v_lshl_or_b32 v169, v40, 4, v42
	v_lshl_or_b32 v168, v38, 4, v41
	v_lshl_add_u64 v[154:155], v[58:59], 0, s[36:37]
	v_lshl_add_u64 v[156:157], v[54:55], 0, s[36:37]
	v_lshl_add_u64 v[158:159], v[56:57], 0, s[36:37]
	v_sub_u32_e32 v176, v4, v150
	v_mov_b32_e32 v54, v3
	v_mov_b32_e32 v55, v3
	v_mov_b32_e32 v56, v3
	v_mov_b32_e32 v57, v3
	v_mov_b32_e32 v58, v3
	v_mov_b32_e32 v59, v3
	v_mov_b32_e32 v60, v3
	v_mov_b32_e32 v61, v3
	v_mov_b32_e32 v62, v3
	v_mov_b32_e32 v63, v3
	v_mov_b32_e32 v64, v3
	v_mov_b32_e32 v65, v3
	v_mov_b32_e32 v66, v3
	v_mov_b32_e32 v67, v3
	v_mov_b64_e32 v[36:37], v[52:53]
	v_mov_b64_e32 v[20:21], v[52:53]
	v_mov_b64_e32 v[4:5], v[52:53]
	s_lshl_b32 s19, s19, 1
	s_or_b32 s24, s16, 31
	s_mov_b32 s25, 0x10000
	s_mov_b32 s31, 0x8000
	s_mov_b32 s0, 0
	s_movk_i32 s34, 0xffc0
	v_mov_b64_e32 v[38:39], v[54:55]
	v_mov_b64_e32 v[40:41], v[56:57]
	v_mov_b64_e32 v[42:43], v[58:59]
	v_mov_b64_e32 v[44:45], v[60:61]
	v_mov_b64_e32 v[46:47], v[62:63]
	v_mov_b64_e32 v[48:49], v[64:65]
	v_mov_b64_e32 v[50:51], v[66:67]
	v_mov_b64_e32 v[22:23], v[54:55]
	v_mov_b64_e32 v[24:25], v[56:57]
	v_mov_b64_e32 v[26:27], v[58:59]
	v_mov_b64_e32 v[28:29], v[60:61]
	v_mov_b64_e32 v[30:31], v[62:63]
	v_mov_b64_e32 v[32:33], v[64:65]
	v_mov_b64_e32 v[34:35], v[66:67]
	v_mov_b64_e32 v[6:7], v[54:55]
	v_mov_b64_e32 v[8:9], v[56:57]
	v_mov_b64_e32 v[10:11], v[58:59]
	v_mov_b64_e32 v[12:13], v[60:61]
	v_mov_b64_e32 v[14:15], v[62:63]
	v_mov_b64_e32 v[16:17], v[64:65]
	v_mov_b64_e32 v[18:19], v[66:67]
	v_readfirstlane_b32 s101, v1
	s_nop 3
	s_bfe_u32 s101, s101, 0x10008
	s_mov_b32 s72, 0
	s_cmp_ge_u32 s72, s19
	s_mov_b32 s73, s0
	s_cbranch_scc1 .LBB0_397
	s_branch .LBB0_396

.LBB0_436:
	s_cmp_eq_u32 s101, 0
	s_cbranch_scc1 .Latt_tail
	s_waitcnt vmcnt(0) lgkmcnt(0)
	s_barrier

.LBB0_439:
	s_cmp_lg_u32 s101, 0
	s_cbranch_scc1 .Latt_bar_done

; __device__ __forceinline__ void attn_unit(LAS unsigned char* lds, const bf16* proj, bf16* Y, const float* relb, const float* hgain, float lam, float oscale, int b, int h, int qb, int tid, int lane, int wid, Stopwatch& sw) {
;     ...
;     for (int t = 0; t < NT; ++t) ATT_TILE(t);
.Latt_bar_done:
	s_add_i32 s72, s72, 1
	v_lshl_add_u64 v[154:155], v[154:155], 0, s[92:93]
	v_lshl_add_u64 v[156:157], v[156:157], 0, s[92:93]
	v_lshl_add_u64 v[158:159], v[158:159], 0, s[92:93]
	v_lshl_add_u64 v[160:161], v[160:161], 0, s[92:93]
	s_cmp_eq_u32 s5, s34
	v_subrev_u32_e32 v176, 64, v176
	s_cbranch_scc0 .LBB0_395
	s_lshl_b32 s0, s19, 6
	s_add_i32 s0, s0, 64
	s_cmp_gt_u32 s0, s24
	s_cbranch_scc1 .LBB0_442
	v_add_u32_e32 v100, s82, v175
	v_add_u32_e32 v101, s82, v174
	v_add_u32_e32 v102, s82, v173
	v_add_u32_e32 v103, s82, v172
	v_add_u32_e32 v104, s82, v171
	v_add_u32_e32 v105, s82, v170
	v_add_u32_e32 v106, s82, v169
	v_add_u32_e32 v107, s82, v168
	ds_read_b64_tr_b16 v[68:69], v100 offset:16384
	ds_read_b64_tr_b16 v[70:71], v101 offset:16384
	ds_read_b64_tr_b16 v[74:75], v101 offset:20480
	ds_read_b64_tr_b16 v[72:73], v100 offset:20480
	ds_read_b64_tr_b16 v[76:77], v102 offset:16384
	ds_read_b64_tr_b16 v[78:79], v103 offset:16384
	ds_read_b64_tr_b16 v[82:83], v103 offset:20480
	ds_read_b64_tr_b16 v[80:81], v102 offset:20480
	ds_read_b64_tr_b16 v[84:85], v104 offset:16384
	ds_read_b64_tr_b16 v[86:87], v105 offset:16384
	ds_read_b64_tr_b16 v[90:91], v105 offset:20480
	ds_read_b64_tr_b16 v[88:89], v104 offset:20480
	ds_read_b64_tr_b16 v[92:93], v106 offset:16384
	ds_read_b64_tr_b16 v[94:95], v107 offset:16384
	ds_read_b64_tr_b16 v[98:99], v107 offset:20480
	ds_read_b64_tr_b16 v[96:97], v106 offset:20480
	s_waitcnt lgkmcnt(14)
	v_mfma_f32_32x32x16_bf16 v[52:67], v[68:71], v[144:147], v[52:67]
	s_waitcnt lgkmcnt(10)
	v_mfma_f32_32x32x16_bf16 v[36:51], v[76:79], v[144:147], v[36:51]
	s_waitcnt lgkmcnt(6)
	v_mfma_f32_32x32x16_bf16 v[20:35], v[84:87], v[144:147], v[20:35]
	s_waitcnt lgkmcnt(2)
	v_mfma_f32_32x32x16_bf16 v[4:19], v[92:95], v[144:147], v[4:19]
	ds_read_b64_tr_b16 v[68:69], v100 offset:24576
	ds_read_b64_tr_b16 v[70:71], v101 offset:24576
	ds_read_b64_tr_b16 v[76:77], v102 offset:24576
	ds_read_b64_tr_b16 v[78:79], v103 offset:24576
	ds_read_b64_tr_b16 v[84:85], v104 offset:24576
	ds_read_b64_tr_b16 v[86:87], v105 offset:24576
	ds_read_b64_tr_b16 v[92:93], v106 offset:24576
	ds_read_b64_tr_b16 v[94:95], v107 offset:24576
	v_mfma_f32_32x32x16_bf16 v[52:67], v[72:75], v[140:143], v[52:67]
	v_mfma_f32_32x32x16_bf16 v[36:51], v[80:83], v[140:143], v[36:51]
	v_mfma_f32_32x32x16_bf16 v[20:35], v[88:91], v[140:143], v[20:35]
	s_waitcnt lgkmcnt(8)
	v_mfma_f32_32x32x16_bf16 v[4:19], v[96:99], v[140:143], v[4:19]
	ds_read_b64_tr_b16 v[72:73], v100 offset:28672
	ds_read_b64_tr_b16 v[74:75], v101 offset:28672
	ds_read_b64_tr_b16 v[80:81], v102 offset:28672
	ds_read_b64_tr_b16 v[82:83], v103 offset:28672
	ds_read_b64_tr_b16 v[88:89], v104 offset:28672
	ds_read_b64_tr_b16 v[90:91], v105 offset:28672
	ds_read_b64_tr_b16 v[96:97], v106 offset:28672
	ds_read_b64_tr_b16 v[98:99], v107 offset:28672
	s_waitcnt lgkmcnt(14)
	v_mfma_f32_32x32x16_bf16 v[52:67], v[68:71], v[132:135], v[52:67]
	s_waitcnt lgkmcnt(12)
	v_mfma_f32_32x32x16_bf16 v[36:51], v[76:79], v[132:135], v[36:51]
	s_waitcnt lgkmcnt(10)
	v_mfma_f32_32x32x16_bf16 v[20:35], v[84:87], v[132:135], v[20:35]
	s_waitcnt lgkmcnt(8)
	v_mfma_f32_32x32x16_bf16 v[4:19], v[92:95], v[132:135], v[4:19]
	s_waitcnt lgkmcnt(6)
	v_mfma_f32_32x32x16_bf16 v[52:67], v[72:75], v[136:139], v[52:67]
	s_waitcnt lgkmcnt(4)
	v_mfma_f32_32x32x16_bf16 v[36:51], v[80:83], v[136:139], v[36:51]
	s_waitcnt lgkmcnt(2)
	v_mfma_f32_32x32x16_bf16 v[20:35], v[88:91], v[136:139], v[20:35]
	s_waitcnt lgkmcnt(0)
	v_mfma_f32_32x32x16_bf16 v[4:19], v[96:99], v[136:139], v[4:19]
